# MLA loop: row-max branch taken after two PV MFMAs, tile-j exps spread over six PV gaps
# speedup vs baseline: 1.0110x; 1.0007x over previous
; __device__ __forceinline__ void finishSM(f32x16& p0, f32x16& p1, float alpha, float& l_reg, bf16x8& pa0, bf16x8& pa1, bf16x8& pa2, bf16x8& pa3) {
; #pragma unroll
;     for (int r = 0; r < 16; ++r) p1[r] = EXP_PROBE ? fmaf(p1[r], 0.001f, 1.f) : __builtin_amdgcn_exp2f(p1[r]);
;     float ps = 0.f;
; #pragma unroll
;     for (int r = 0; r < 16; ++r) ps += p0[r];
; #pragma unroll
;     for (int r = 0; r < 16; ++r) ps += p1[r];
;     { auto rr = __builtin_amdgcn_permlane32_swap(__float_as_uint(ps), __float_as_uint(ps), false, false);
;       ps = __uint_as_float(rr[0]) + __uint_as_float(rr[1]); }
;     l_reg = l_reg * alpha + ps;
;     ATT_PKN(p0, 0, pa0); ATT_PKN(p0, 8, pa1); ATT_PKN(p1, 0, pa2); ATT_PKN(p1, 8, pa3);
; }
; template <int DQK> __device__ __forceinline__ void qkt(f32x16& p0, f32x16& p1, const LAS char* buf, const bf16x8* qr, int r32, int hi, const f32x16& negm) {
; #pragma unroll
;     for (int d0 = 0; d0 < 4; ++d0) { const int ch = d0 * 2 + hi;
;         const bf16x8 b0 = *(const LAS bf16x8*)(buf + B_KN + swz64(r32, ch));
;         const bf16x8 b1 = *(const LAS bf16x8*)(buf + B_KN + swz64(32 + r32, ch));
;         p0 = __builtin_amdgcn_mfma_f32_32x32x16_bf16(b0, qr[d0], d0 == 0 ? negm : p0, 0, 0, 0);
;         p1 = __builtin_amdgcn_mfma_f32_32x32x16_bf16(b1, qr[d0], d0 == 0 ? negm : p1, 0, 0, 0); }
;     if constexpr (DQK == 96) {
; #pragma unroll
;         for (int d0 = 0; d0 < 2; ++d0) { const int ch = d0 * 2 + hi;
;             const bf16x8 b0 = *(const LAS bf16x8*)(buf + B_KR + swz32(r32, ch));
;             const bf16x8 b1 = *(const LAS bf16x8*)(buf + B_KR + swz32(32 + r32, ch));
;             p0 = __builtin_amdgcn_mfma_f32_32x32x16_bf16(b0, qr[4 + d0], p0, 0, 0, 0);
;             p1 = __builtin_amdgcn_mfma_f32_32x32x16_bf16(b1, qr[4 + d0], p1, 0, 0, 0); }
;     }
; }
; template <int D0> __device__ __forceinline__ void pv_one(f32x16& od, unsigned vb, bf16x8 pa0, bf16x8 pa1, bf16x8 pa2, bf16x8 pa3) {
;     const s16x4 l0 = tr_read<v_rd_off(D0, 0, 0)>(vb), h0 = tr_read<v_rd_off(D0, 0, 1)>(vb), l1 = tr_read<v_rd_off(D0, 1, 0)>(vb), h1 = tr_read<v_rd_off(D0, 1, 1)>(vb);
;     const s16x4 l2 = tr_read<v_rd_off(D0, 2, 0)>(vb), h2 = tr_read<v_rd_off(D0, 2, 1)>(vb), l3 = tr_read<v_rd_off(D0, 3, 0)>(vb), h3 = tr_read<v_rd_off(D0, 3, 1)>(vb);
;     asm volatile("s_waitcnt lgkmcnt(0)" ::: "memory"); SBAR();
.LBB0_523:
	s_mov_b32 s10, s0
	s_waitcnt lgkmcnt(0)
	s_barrier
	v_add_u32_e32 v2, s13, v201
	v_add_u32_e32 v8, v2, v209
	ds_read_b128 v[4:7], v8
	ds_read_b128 v[8:11], v8 offset:4096
	v_add_u32_e32 v246, v2, v210
	ds_read_b128 v[174:177], v246
	ds_read_b128 v[246:249], v246 offset:4096
	v_add_u32_e32 v78, v2, v211
	ds_read_b128 v[250:253], v78
	ds_read_b128 v[78:81], v78 offset:4096
	v_add_u32_e32 v16, v2, v212
	ds_read_b128 v[12:15], v16
	v_add_u32_e32 v2, s13, v217
	v_exp_f32_e32 v98, v98
	v_exp_f32_e32 v99, v99
	v_exp_f32_e32 v100, v100
	v_exp_f32_e32 v101, v101
	v_exp_f32_e32 v102, v102
	v_exp_f32_e32 v103, v103
	v_exp_f32_e32 v104, v104
	v_exp_f32_e32 v105, v105
	s_waitcnt lgkmcnt(6)
	v_mfma_f32_32x32x16_bf16 v[130:145], v[4:7], v[166:169], v[82:97]
	ds_read_b128 v[4:7], v16 offset:4096
	v_exp_f32_e32 v106, v106
	v_exp_f32_e32 v107, v107
	v_exp_f32_e32 v108, v108
	v_cvt_pk_bf16_f32 v74, v243, v245
	s_waitcnt lgkmcnt(6)
	v_mfma_f32_32x32x16_bf16 v[114:129], v[8:11], v[166:169], v[82:97]
	v_add_u32_e32 v16, v2, v219
	ds_read_b128 v[8:11], v16 offset:8192
	v_exp_f32_e32 v109, v109
	v_exp_f32_e32 v110, v110
	v_exp_f32_e32 v111, v111
	v_cvt_pk_bf16_f32 v75, v241, v244
	s_waitcnt lgkmcnt(6)
	v_mfma_f32_32x32x16_bf16 v[130:145], v[174:177], v[162:165], v[130:145]
	ds_read_b128 v[174:177], v16 offset:10240
	v_exp_f32_e32 v112, v112
	v_exp_f32_e32 v113, v113
	v_cvt_pk_bf16_f32 v76, v239, v242
	v_cvt_pk_bf16_f32 v77, v238, v240
	v_add_f32_e32 v229, 0, v243
	v_add_f32_e32 v229, v245, v229
	s_waitcnt lgkmcnt(6)
	v_mfma_f32_32x32x16_bf16 v[114:129], v[246:249], v[162:165], v[114:129]
	v_add_u32_e32 v16, v2, v220
	ds_read_b128 v[246:249], v16 offset:8192
	v_cvt_pk_bf16_f32 v66, v236, v237
	v_cvt_pk_bf16_f32 v67, v233, v235
	v_add_f32_e32 v229, v241, v229
	v_add_f32_e32 v229, v244, v229
	v_add_f32_e32 v229, v239, v229
	v_add_f32_e32 v229, v242, v229
	s_waitcnt lgkmcnt(6)
	v_mfma_f32_32x32x16_bf16 v[130:145], v[250:253], v[158:161], v[130:145]
	ds_read_b128 v[250:253], v16 offset:10240
	v_cvt_pk_bf16_f32 v68, v231, v234
	v_cvt_pk_bf16_f32 v69, v230, v232
	v_add_f32_e32 v229, v238, v229
	v_add_f32_e32 v229, v240, v229
	v_add_f32_e32 v229, v236, v229
	v_add_f32_e32 v229, v237, v229
	s_waitcnt lgkmcnt(6)
	v_mfma_f32_32x32x16_bf16 v[114:129], v[78:81], v[158:161], v[114:129]
	v_add_f32_e32 v229, v233, v229
	v_add_f32_e32 v229, v235, v229
	v_add_f32_e32 v229, v231, v229
	v_add_f32_e32 v229, v234, v229
	v_add_f32_e32 v229, v230, v229
	v_add_f32_e32 v229, v232, v229
	s_waitcnt lgkmcnt(5)
	v_mfma_f32_32x32x16_bf16 v[130:145], v[12:15], v[154:157], v[130:145]
	v_add_u32_e32 v17, s11, v213
	ds_read_b64_tr_b16 v[230:231], v17 offset:0
	ds_read_b64_tr_b16 v[232:233], v17 offset:1024
	ds_read_b64_tr_b16 v[234:235], v17 offset:2048
	ds_read_b64_tr_b16 v[236:237], v17 offset:3072
	v_add_f32_e32 v229, v98, v229
	v_add_f32_e32 v229, v99, v229
	v_add_f32_e32 v229, v100, v229
	s_waitcnt lgkmcnt(8)
	v_mfma_f32_32x32x16_bf16 v[114:129], v[4:7], v[154:157], v[114:129]
	ds_read_b64_tr_b16 v[238:239], v17 offset:4096
	ds_read_b64_tr_b16 v[240:241], v17 offset:5120
	ds_read_b64_tr_b16 v[242:243], v17 offset:6144
	ds_read_b64_tr_b16 v[244:245], v17 offset:7168
	v_add_f32_e32 v229, v101, v229
	v_add_f32_e32 v229, v102, v229
	v_add_f32_e32 v229, v103, v229
	s_waitcnt lgkmcnt(11)
	v_mfma_f32_32x32x16_bf16 v[130:145], v[8:11], v[150:153], v[130:145]
	v_add_f32_e32 v229, v104, v229
	v_add_f32_e32 v229, v105, v229
	v_add_f32_e32 v229, v106, v229
	v_add_f32_e32 v229, v107, v229
	v_add_f32_e32 v229, v108, v229
	v_add_f32_e32 v229, v109, v229
	s_waitcnt lgkmcnt(10)
	v_mfma_f32_32x32x16_bf16 v[114:129], v[174:177], v[150:153], v[114:129]
	v_add_f32_e32 v229, v110, v229
	v_add_f32_e32 v229, v111, v229
	v_add_f32_e32 v229, v112, v229
	v_add_f32_e32 v228, v113, v229
	v_mov_b32_e32 v229, v228
	s_add_i32 s36, s35, -1
	s_cmp_lt_u32 s36, s30
	s_cselect_b32 s0, 0, s30
	s_cselect_b32 s1, s29, s34
	s_lshl_b32 s0, s0, 6
	s_sub_i32 s37, s1, s0
	s_lshl_b32 s1, s36, 6
	s_add_i32 s37, s37, s1
	s_lshl_b32 s0, s37, 6
	s_add_u32 s48, s44, s0
	s_addc_u32 s49, s45, 0
	s_lshl_b32 s0, s37, 11
	s_add_u32 s46, s42, s0
	s_addc_u32 s47, s43, 0
	global_load_dwordx4 v[174:177], v226, s[48:49]
	s_waitcnt lgkmcnt(9)
	v_mfma_f32_32x32x16_bf16 v[130:145], v[246:249], v[146:149], v[130:145]
	v_cvt_pk_bf16_f32 v70, v98, v99
	v_cvt_pk_bf16_f32 v71, v100, v101
	v_cvt_pk_bf16_f32 v72, v102, v103
	v_cvt_pk_bf16_f32 v73, v104, v105
	v_permlane32_swap_b32_e32 v228, v229
	global_load_dwordx4 v[8:11], v225, s[46:47]
	global_load_dwordx4 v[4:7], v225, s[46:47] offset:128
	s_waitcnt lgkmcnt(8)
	v_mfma_f32_32x32x16_bf16 v[114:129], v[250:253], v[146:149], v[114:129]
	v_cvt_pk_bf16_f32 v12, v106, v107
	v_cvt_pk_bf16_f32 v13, v108, v109
	v_cvt_pk_bf16_f32 v14, v110, v111
	v_cvt_pk_bf16_f32 v15, v112, v113
	ds_read_b64_tr_b16 v[78:79], v17 offset:512
	ds_read_b64_tr_b16 v[80:81], v17 offset:1536
	ds_read_b64_tr_b16 v[98:99], v17 offset:2560
	ds_read_b64_tr_b16 v[100:101], v17 offset:3584
	ds_read_b64_tr_b16 v[102:103], v17 offset:4608
	ds_read_b64_tr_b16 v[104:105], v17 offset:5632
	ds_read_b64_tr_b16 v[110:111], v17 offset:6656
	ds_read_b64_tr_b16 v[112:113], v17 offset:7680
	v_max3_f32 v2, v130, v131, v132
	v_max3_f32 v2, v2, v133, v134
	v_max3_f32 v2, v2, v135, v136
	v_max3_f32 v2, v2, v137, v138
	v_max3_f32 v2, v2, v139, v140
	v_max3_f32 v2, v2, v141, v142
	v_max3_f32 v2, v2, v143, v144
	v_max3_f32 v2, v2, v145, v114
	v_max3_f32 v2, v2, v115, v116
	v_max3_f32 v2, v2, v117, v118
	v_max3_f32 v2, v2, v119, v120
	v_max3_f32 v2, v2, v121, v122
	s_waitcnt lgkmcnt(8)
	v_mfma_f32_32x32x16_bf16 v[50:65], v[230:233], v[74:77], v[50:65]
	v_max3_f32 v2, v2, v123, v124
	v_max3_f32 v2, v2, v125, v126
	v_max3_f32 v2, v2, v127, v128
	v_max_f32_e32 v2, v2, v129
	s_nop 0
	s_nop 0
	v_mov_b32_e32 v16, v2
	v_mfma_f32_32x32x16_bf16 v[50:65], v[234:237], v[66:69], v[50:65]
	s_nop 1
	v_permlane32_swap_b32_e32 v2, v16
	v_max_f32_e32 v2, v2, v16
	v_cmp_ge_f32_e32 vcc, s28, v2
	s_cmp_eq_u64 vcc, exec
	s_cbranch_scc0 .LBB0_542
	v_mov_b32_e32 v2, 1.0
; #define SBAR() __builtin_amdgcn_sched_barrier(0)
; template <bool FIRST> __device__ __forceinline__ void psm_apply(f32x16& p0, f32x16& p1, float pmax, float& m_reg, f32x16& negm, float& alpha) {
;     alpha = 1.f;
;     if (FIRST || !__builtin_expect(__all(pmax <= THR2), 1)) {
;         const float delta = FIRST ? pmax : fmaxf(pmax, 0.f);
;         if (!FIRST) alpha = __builtin_amdgcn_exp2f(-delta);
;         m_reg += delta;
; #pragma unroll
;         for (int r = 0; r < 16; ++r) { p0[r] -= delta; p1[r] -= delta; negm[r] = -m_reg; }
;     }
; #pragma unroll
;     for (int r = 0; r < 16; ++r) p0[r] = EXP_PROBE ? fmaf(p0[r], 0.001f, 1.f) : __builtin_amdgcn_exp2f(p0[r]);
; }
; template <int D0> __device__ __forceinline__ void pv_one(f32x16& od, unsigned vb, bf16x8 pa0, bf16x8 pa1, bf16x8 pa2, bf16x8 pa3) {
;     const s16x4 l0 = tr_read<v_rd_off(D0, 0, 0)>(vb), h0 = tr_read<v_rd_off(D0, 0, 1)>(vb), l1 = tr_read<v_rd_off(D0, 1, 0)>(vb), h1 = tr_read<v_rd_off(D0, 1, 1)>(vb);
;     const s16x4 l2 = tr_read<v_rd_off(D0, 2, 0)>(vb), h2 = tr_read<v_rd_off(D0, 2, 1)>(vb), l3 = tr_read<v_rd_off(D0, 3, 0)>(vb), h3 = tr_read<v_rd_off(D0, 3, 1)>(vb);
;     asm volatile("s_waitcnt lgkmcnt(0)" ::: "memory"); SBAR();
;     ...
;     od = __builtin_amdgcn_mfma_f32_32x32x16_bf16(ATT_PK(l0, h0), pa0, od, 0, 0, 0);
;     od = __builtin_amdgcn_mfma_f32_32x32x16_bf16(ATT_PK(l1, h1), pa1, od, 0, 0, 0);
;     od = __builtin_amdgcn_mfma_f32_32x32x16_bf16(ATT_PK(l2, h2), pa2, od, 0, 0, 0);
;     od = __builtin_amdgcn_mfma_f32_32x32x16_bf16(ATT_PK(l3, h3), pa3, od, 0, 0, 0);
.LBB0_527:
	v_mfma_f32_32x32x16_bf16 v[50:65], v[238:241], v[70:73], v[50:65]
	v_exp_f32_e32 v16, v130
	v_exp_f32_e32 v234, v131
	v_exp_f32_e32 v235, v132
	v_mfma_f32_32x32x16_bf16 v[50:65], v[242:245], v[12:15], v[50:65]
	v_exp_f32_e32 v236, v133
	v_exp_f32_e32 v237, v134
	v_exp_f32_e32 v238, v135
	s_waitcnt lgkmcnt(0)
	v_mfma_f32_32x32x16_bf16 v[34:49], v[78:81], v[74:77], v[34:49]
	s_waitcnt vmcnt(3)
	v_add_u32_e32 v17, s10, v187
	ds_write_b128 v17, v[178:181]
	v_add_u32_e32 v17, s10, v214
	ds_write_b128 v17, v[182:185] offset:12288
	s_cmp_eq_u64 s[2:3], 0
	s_cbranch_scc1 .Lmla_a_nokr
	v_add_u32_e32 v17, s10, v216
	ds_write_b128 v17, v[170:173] offset:8192
.Lmla_a_nokr:
	v_exp_f32_e32 v239, v136
	v_exp_f32_e32 v240, v137
	v_mfma_f32_32x32x16_bf16 v[34:49], v[98:101], v[66:69], v[34:49]
	v_exp_f32_e32 v241, v138
	v_exp_f32_e32 v242, v139
	v_exp_f32_e32 v243, v140
	v_mfma_f32_32x32x16_bf16 v[34:49], v[102:105], v[70:73], v[34:49]
	v_exp_f32_e32 v244, v141
	v_exp_f32_e32 v245, v142
	v_exp_f32_e32 v246, v143
	v_mfma_f32_32x32x16_bf16 v[34:49], v[110:113], v[12:15], v[34:49]
	v_exp_f32_e32 v247, v144
	v_exp_f32_e32 v248, v145
	v_cmp_gt_f32_e32 vcc, 1.0, v2
	s_cbranch_vccz .LBB0_531
	s_nop 7
	s_nop 7
	v_pk_mul_f32 v[64:65], v[64:65], v[2:3] op_sel_hi:[1,0]
	v_pk_mul_f32 v[62:63], v[62:63], v[2:3] op_sel_hi:[1,0]
	v_pk_mul_f32 v[60:61], v[60:61], v[2:3] op_sel_hi:[1,0]
	v_pk_mul_f32 v[58:59], v[58:59], v[2:3] op_sel_hi:[1,0]
	v_pk_mul_f32 v[56:57], v[56:57], v[2:3] op_sel_hi:[1,0]
	v_pk_mul_f32 v[54:55], v[54:55], v[2:3] op_sel_hi:[1,0]
	v_pk_mul_f32 v[52:53], v[52:53], v[2:3] op_sel_hi:[1,0]
	v_pk_mul_f32 v[50:51], v[50:51], v[2:3] op_sel_hi:[1,0]
	v_pk_mul_f32 v[48:49], v[48:49], v[2:3] op_sel_hi:[1,0]
	v_pk_mul_f32 v[46:47], v[46:47], v[2:3] op_sel_hi:[1,0]
	v_pk_mul_f32 v[44:45], v[44:45], v[2:3] op_sel_hi:[1,0]
	v_pk_mul_f32 v[42:43], v[42:43], v[2:3] op_sel_hi:[1,0]
	v_pk_mul_f32 v[40:41], v[40:41], v[2:3] op_sel_hi:[1,0]
	v_pk_mul_f32 v[38:39], v[38:39], v[2:3] op_sel_hi:[1,0]
	v_pk_mul_f32 v[36:37], v[36:37], v[2:3] op_sel_hi:[1,0]
	v_pk_mul_f32 v[34:35], v[34:35], v[2:3] op_sel_hi:[1,0]

; #define SBAR() __builtin_amdgcn_sched_barrier(0)
; __device__ __forceinline__ float psm_max(const f32x16& p0, const f32x16& p1) {
;     float pmax = p0[0];
; #pragma unroll
;     for (int r = 1; r < 16; ++r) pmax = fmaxf(pmax, p0[r]);
; #pragma unroll
;     for (int r = 0; r < 16; ++r) pmax = fmaxf(pmax, p1[r]);
;     { auto rr = __builtin_amdgcn_permlane32_swap(__float_as_uint(pmax), __float_as_uint(pmax), false, false);
;       pmax = fmaxf(__uint_as_float(rr[0]), __uint_as_float(rr[1])); }
;     return pmax;
; }
; template <bool FIRST> __device__ __forceinline__ void psm_apply(f32x16& p0, f32x16& p1, float pmax, float& m_reg, f32x16& negm, float& alpha) {
;     alpha = 1.f;
;     if (FIRST || !__builtin_expect(__all(pmax <= THR2), 1)) {
;         const float delta = FIRST ? pmax : fmaxf(pmax, 0.f);
;         if (!FIRST) alpha = __builtin_amdgcn_exp2f(-delta);
;         m_reg += delta;
; #pragma unroll
;         for (int r = 0; r < 16; ++r) { p0[r] -= delta; p1[r] -= delta; negm[r] = -m_reg; }
;     }
; #pragma unroll
;     for (int r = 0; r < 16; ++r) p0[r] = EXP_PROBE ? fmaf(p0[r], 0.001f, 1.f) : __builtin_amdgcn_exp2f(p0[r]);
; }
; template <int D0> __device__ __forceinline__ void pv_one(f32x16& od, unsigned vb, bf16x8 pa0, bf16x8 pa1, bf16x8 pa2, bf16x8 pa3) {
;     const s16x4 l0 = tr_read<v_rd_off(D0, 0, 0)>(vb), h0 = tr_read<v_rd_off(D0, 0, 1)>(vb), l1 = tr_read<v_rd_off(D0, 1, 0)>(vb), h1 = tr_read<v_rd_off(D0, 1, 1)>(vb);
;     const s16x4 l2 = tr_read<v_rd_off(D0, 2, 0)>(vb), h2 = tr_read<v_rd_off(D0, 2, 1)>(vb), l3 = tr_read<v_rd_off(D0, 3, 0)>(vb), h3 = tr_read<v_rd_off(D0, 3, 1)>(vb);
;     asm volatile("s_waitcnt lgkmcnt(0)" ::: "memory"); SBAR();
;     ...
;     od = __builtin_amdgcn_mfma_f32_32x32x16_bf16(ATT_PK(l0, h0), pa0, od, 0, 0, 0);
;     od = __builtin_amdgcn_mfma_f32_32x32x16_bf16(ATT_PK(l1, h1), pa1, od, 0, 0, 0);
;     od = __builtin_amdgcn_mfma_f32_32x32x16_bf16(ATT_PK(l2, h2), pa2, od, 0, 0, 0);
;     od = __builtin_amdgcn_mfma_f32_32x32x16_bf16(ATT_PK(l3, h3), pa3, od, 0, 0, 0);
.Lmla_b_ld_done:
	s_waitcnt lgkmcnt(8)
	v_mfma_f32_32x32x16_bf16 v[98:113], v[70:73], v[146:149], v[98:113]
	v_cvt_pk_bf16_f32 v118, v122, v123
	v_cvt_pk_bf16_f32 v119, v124, v125
	v_cvt_pk_bf16_f32 v120, v126, v127
	v_cvt_pk_bf16_f32 v121, v128, v129
	v_add_f32_e32 v126, v129, v252
	v_mov_b32_e32 v127, v126
	ds_read_b64_tr_b16 v[66:67], v16 offset:512
	ds_read_b64_tr_b16 v[68:69], v16 offset:1536
	ds_read_b64_tr_b16 v[70:71], v16 offset:2560
	ds_read_b64_tr_b16 v[72:73], v16 offset:3584
	ds_read_b64_tr_b16 v[74:75], v16 offset:4608
	ds_read_b64_tr_b16 v[76:77], v16 offset:5632
	ds_read_b64_tr_b16 v[78:79], v16 offset:6656
	ds_read_b64_tr_b16 v[80:81], v16 offset:7680
	v_permlane32_swap_b32_e32 v126, v127
	v_max3_f32 v250, v130, v131, v132
	v_max3_f32 v250, v250, v133, v134
	v_max3_f32 v250, v250, v135, v136
	v_max3_f32 v250, v250, v137, v138
	v_max3_f32 v250, v250, v139, v140
	v_max3_f32 v250, v250, v141, v142
	v_max3_f32 v250, v250, v143, v144
	v_max3_f32 v250, v250, v145, v98
	v_max3_f32 v250, v250, v99, v100
	v_max3_f32 v250, v250, v101, v102
	v_max3_f32 v250, v250, v103, v104
	v_max3_f32 v250, v250, v105, v106
	s_waitcnt lgkmcnt(8)
	v_mfma_f32_32x32x16_bf16 v[50:65], v[234:237], v[12:15], v[50:65]
	v_max3_f32 v250, v250, v107, v108
	v_max3_f32 v250, v250, v109, v110
	v_max3_f32 v250, v250, v111, v112
	v_max_f32_e32 v250, v250, v113
	s_nop 0
	s_nop 0
	v_mov_b32_e32 v251, v250
	v_mfma_f32_32x32x16_bf16 v[50:65], v[238:241], v[230:233], v[50:65]
	s_nop 1
	v_permlane32_swap_b32_e32 v250, v251
	v_max_f32_e32 v250, v250, v251
	v_cmp_ge_f32_e32 vcc, s28, v250
	s_cmp_eq_u64 vcc, exec
	v_mov_b32_e32 v16, 1.0
	s_cbranch_scc0 .LBB0_543
.LBB0_536:
	v_mfma_f32_32x32x16_bf16 v[50:65], v[242:245], v[114:117], v[50:65]
	v_exp_f32_e32 v243, v130
	v_exp_f32_e32 v245, v131
	v_exp_f32_e32 v241, v132
	v_mfma_f32_32x32x16_bf16 v[50:65], v[246:249], v[118:121], v[50:65]
	v_exp_f32_e32 v244, v133
	v_exp_f32_e32 v239, v134
	v_exp_f32_e32 v242, v135
	s_waitcnt lgkmcnt(0)
	v_mfma_f32_32x32x16_bf16 v[34:49], v[66:69], v[12:15], v[34:49]
	s_waitcnt vmcnt(3)
	v_add_u32_e32 v253, s11, v187
	ds_write_b128 v253, v[8:11]
	v_add_u32_e32 v253, s11, v214
	ds_write_b128 v253, v[4:7] offset:12288
	s_cmp_eq_u64 s[2:3], 0
	s_cbranch_scc1 .Lmla_b_nokr
	v_add_u32_e32 v253, s11, v216
	ds_write_b128 v253, v[174:177] offset:8192
.Lmla_b_nokr:
	v_exp_f32_e32 v238, v136
	v_exp_f32_e32 v240, v137
	v_mfma_f32_32x32x16_bf16 v[34:49], v[70:73], v[230:233], v[34:49]
	v_exp_f32_e32 v236, v138
	v_exp_f32_e32 v237, v139
	v_exp_f32_e32 v235, v141
	v_mfma_f32_32x32x16_bf16 v[34:49], v[74:77], v[114:117], v[34:49]
	v_exp_f32_e32 v234, v143
	v_exp_f32_e32 v233, v140
	v_exp_f32_e32 v231, v142
	v_mfma_f32_32x32x16_bf16 v[34:49], v[78:81], v[118:121], v[34:49]
	v_exp_f32_e32 v230, v144
	v_exp_f32_e32 v232, v145
	v_cmp_gt_f32_e32 vcc, 1.0, v16
	s_cbranch_vccz .LBB0_540
	s_nop 7
	s_nop 7
	v_pk_mul_f32 v[64:65], v[64:65], v[16:17] op_sel_hi:[1,0]
	v_pk_mul_f32 v[62:63], v[62:63], v[16:17] op_sel_hi:[1,0]
	v_pk_mul_f32 v[60:61], v[60:61], v[16:17] op_sel_hi:[1,0]
	v_pk_mul_f32 v[58:59], v[58:59], v[16:17] op_sel_hi:[1,0]
	v_pk_mul_f32 v[56:57], v[56:57], v[16:17] op_sel_hi:[1,0]
	v_pk_mul_f32 v[54:55], v[54:55], v[16:17] op_sel_hi:[1,0]
	v_pk_mul_f32 v[52:53], v[52:53], v[16:17] op_sel_hi:[1,0]
	v_pk_mul_f32 v[50:51], v[50:51], v[16:17] op_sel_hi:[1,0]
	v_pk_mul_f32 v[48:49], v[48:49], v[16:17] op_sel_hi:[1,0]
	v_pk_mul_f32 v[46:47], v[46:47], v[16:17] op_sel_hi:[1,0]
	v_pk_mul_f32 v[44:45], v[44:45], v[16:17] op_sel_hi:[1,0]
	v_pk_mul_f32 v[42:43], v[42:43], v[16:17] op_sel_hi:[1,0]
	v_pk_mul_f32 v[40:41], v[40:41], v[16:17] op_sel_hi:[1,0]
	v_pk_mul_f32 v[38:39], v[38:39], v[16:17] op_sel_hi:[1,0]
	v_pk_mul_f32 v[36:37], v[36:37], v[16:17] op_sel_hi:[1,0]
	v_pk_mul_f32 v[34:35], v[34:35], v[16:17] op_sel_hi:[1,0]
